# baseline (speedup 1.0000x reference)
_Z11attn_kernelPKDF16_S0_PDF16_P15HIP_vector_typeIfLj2EE:
	s_lshl_b32 s40, s3, 4
	s_add_u32 s40, s40, s2
	s_lshl_b32 s41, s4, 6
	s_add_u32 s40, s40, s41
	s_and_b32 s41, s40, 7
	s_lshr_b32 s40, s40, 3
	s_and_b32 s2, s41, 3
	s_lshl_b32 s2, s2, 2
	s_and_b32 s3, s40, 3
	s_or_b32 s2, s2, s3
	s_lshr_b32 s3, s40, 2
	s_and_b32 s3, s3, 3
	s_lshr_b32 s4, s41, 2
	s_lshl_b32 s4, s4, 1
	s_lshr_b32 s40, s40, 4
	s_or_b32 s4, s4, s40
	s_getpc_b64 s[38:39]
	v_lshlrev_b32_e32 v240, 7, v0
	v_min_u32_e32 v240, 0x3380, v240
	global_load_dword v241, v240, s[38:39]
	s_mov_b32 s5, 0
	s_mov_b32 s28, s3
	s_load_dwordx8 s[20:27], s[0:1], 0x0
	s_mov_b32 s3, s5
	s_lshl_b64 s[0:1], s[4:5], 12
	s_lshl_b64 s[2:3], s[2:3], 8
	s_add_u32 s0, s0, s2
	v_lshrrev_b32_e32 v1, 6, v0
	s_addc_u32 s1, s1, s3
	v_and_b32_e32 v160, 31, v0
	s_lshl_b64 s[2:3], s[0:1], 8
	v_lshlrev_b32_e32 v162, 5, v1
	s_waitcnt lgkmcnt(0)
	s_add_u32 s2, s20, s2
	v_or_b32_e32 v2, v162, v160
	v_bfe_u32 v54, v0, 5, 1
	s_addc_u32 s3, s21, s3
	v_and_b32_e32 v164, 63, v0
	v_lshrrev_b32_e32 v165, 4, v164
	v_add_u32_e32 v165, v162, v165
	v_lshlrev_b32_e32 v165, 8, v165
	v_and_b32_e32 v164, 15, v164
	v_lshl_add_u32 v164, v164, 4, v165
	v_mov_b32_e32 v165, 0
	v_lshl_add_u64 v[2:3], s[2:3], 0, v[164:165]
	s_mov_b64 s[6:7], 0x1000
	v_lshl_add_u64 v[4:5], v[2:3], 0, s[6:7]
	global_load_dwordx4 v[156:159], v[2:3], off
	global_load_dwordx4 v[152:155], v[2:3], off offset:1024
	global_load_dwordx4 v[148:151], v[2:3], off offset:2048
	global_load_dwordx4 v[144:147], v[2:3], off offset:3072
	global_load_dwordx4 v[140:143], v[4:5], off
	global_load_dwordx4 v[136:139], v[4:5], off offset:1024
	global_load_dwordx4 v[132:135], v[4:5], off offset:2048
	global_load_dwordx4 v[128:131], v[4:5], off offset:3072
	v_lshlrev_b32_e32 v164, 4, v54
	s_ashr_i32 s29, s28, 31
	v_bfe_u32 v55, v0, 2, 3
	s_lshl_b64 s[2:3], s[4:5], 20
	s_lshl_b64 s[20:21], s[28:29], 18
	v_lshl_or_b32 v2, v1, 3, v55
	s_add_u32 s4, s22, s2
	v_lshrrev_b32_e32 v3, 2, v2
	s_addc_u32 s7, s23, s3
	v_xor_b32_e32 v4, v3, v0
	s_add_u32 s6, s4, s20
	v_and_b32_e32 v5, 32, v0
	v_lshlrev_b32_e32 v4, 3, v4
	v_lshlrev_b32_e32 v1, 11, v1
	s_addc_u32 s7, s7, s21
	v_lshlrev_b32_e32 v164, 8, v2
	v_and_or_b32 v4, v4, 24, v5
	v_add_u32_e32 v173, 0, v1
	v_lshl_add_u64 v[2:3], s[6:7], 0, v[164:165]
	v_lshlrev_b32_e32 v164, 1, v4
	v_readfirstlane_b32 s4, v173
	v_add_u32_e32 v6, 0x400, v173
	v_lshl_add_u64 v[2:3], v[2:3], 0, v[164:165]
	s_mov_b64 s[6:7], 0x80
	s_mov_b32 m0, s4
	v_readfirstlane_b32 s4, v6
	v_add_u32_e32 v6, 0x4000, v173
	v_lshl_add_u64 v[4:5], v[2:3], 0, s[6:7]
	global_load_lds_dwordx4 v[2:3], off
	s_mov_b32 m0, s4
	s_mov_b64 s[6:7], 0x4000
	v_readfirstlane_b32 s4, v6
	global_load_lds_dwordx4 v[4:5], off
	v_lshl_add_u64 v[4:5], v[2:3], 0, s[6:7]
	s_mov_b32 m0, s4
	s_mov_b64 s[6:7], 0x4080
	global_load_lds_dwordx4 v[4:5], off
	v_add_u32_e32 v4, 0x4400, v173
	v_lshl_add_u64 v[2:3], v[2:3], 0, s[6:7]
	v_readfirstlane_b32 s4, v4
	s_mov_b32 m0, s4
	s_movk_i32 s4, 0x1c0
	global_load_lds_dwordx4 v[2:3], off
	v_lshlrev_b32_e32 v2, 8, v0
	v_and_b32_e32 v2, 0x1800, v2
	v_lshlrev_b32_e32 v3, 6, v0
	v_and_or_b32 v6, v3, s4, v2
	v_xor_b32_e32 v2, v54, v55
	v_lshlrev_b32_e32 v2, 4, v2
	v_and_or_b32 v175, v2, 48, v6
	v_and_b32_e32 v190, 63, v0
	v_lshrrev_b32_e32 v191, 4, v190
	v_and_b32_e32 v192, 15, v190
	v_xor_b32_e32 v193, v192, v191
	v_lshlrev_b32_e32 v193, 4, v193
	v_add_u32_e32 v194, v162, v191
	v_lshlrev_b32_e32 v194, 8, v194
	v_add_u32_e32 v194, 0x10000, v194
	v_and_b32_e32 v195, 15, v160
	v_xor_b32_e32 v195, v195, v54
	v_lshlrev_b32_e32 v195, 4, v195
	v_add_u32_e32 v196, v162, v160
	v_lshlrev_b32_e32 v196, 8, v196
	v_add_u32_e32 v196, 0x10000, v196
	s_waitcnt vmcnt(4)
	v_xor_b32_e32 v197, 0x0, v193
	v_add_u32_e32 v197, v197, v194
	ds_write_b128 v197, v[156:159] offset:0
	v_xor_b32_e32 v197, 0x40, v193
	v_add_u32_e32 v197, v197, v194
	ds_write_b128 v197, v[152:155] offset:1024
	v_xor_b32_e32 v197, 0x80, v193
	v_add_u32_e32 v197, v197, v194
	ds_write_b128 v197, v[148:151] offset:2048
	v_xor_b32_e32 v197, 0xc0, v193
	v_add_u32_e32 v197, v197, v194
	ds_write_b128 v197, v[144:147] offset:3072
	v_xor_b32_e32 v197, 0x0, v193
	v_add_u32_e32 v197, v197, v194
	ds_write_b128 v197, v[140:143] offset:4096
	v_xor_b32_e32 v197, 0x40, v193
	v_add_u32_e32 v197, v197, v194
	ds_write_b128 v197, v[136:139] offset:5120
	v_xor_b32_e32 v197, 0x80, v193
	v_add_u32_e32 v197, v197, v194
	ds_write_b128 v197, v[132:135] offset:6144
	v_xor_b32_e32 v197, 0xc0, v193
	v_add_u32_e32 v197, v197, v194
	ds_write_b128 v197, v[128:131] offset:7168
	s_waitcnt lgkmcnt(0)
	v_xor_b32_e32 v198, 0x0, v195
	v_add_u32_e32 v198, v198, v196
	ds_read_b128 v[156:159], v198
	v_xor_b32_e32 v198, 0x20, v195
	v_add_u32_e32 v198, v198, v196
	ds_read_b128 v[152:155], v198
	v_xor_b32_e32 v198, 0x40, v195
	v_add_u32_e32 v198, v198, v196
	ds_read_b128 v[148:151], v198
	v_xor_b32_e32 v198, 0x60, v195
	v_add_u32_e32 v198, v198, v196
	ds_read_b128 v[144:147], v198
	v_xor_b32_e32 v198, 0x80, v195
	v_add_u32_e32 v198, v198, v196
	ds_read_b128 v[140:143], v198
	v_xor_b32_e32 v198, 0xa0, v195
	v_add_u32_e32 v198, v198, v196
	ds_read_b128 v[136:139], v198
	v_xor_b32_e32 v198, 0xc0, v195
	v_add_u32_e32 v198, v198, v196
	ds_read_b128 v[132:135], v198
	v_xor_b32_e32 v198, 0xe0, v195
	v_add_u32_e32 v198, v198, v196
	ds_read_b128 v[128:131], v198
	s_waitcnt vmcnt(2)
	v_add_u32_e32 v172, 0, v175
	s_waitcnt lgkmcnt(0)
	s_barrier
	ds_read_b128 v[2:5], v172
	ds_read_b128 v[34:37], v172 offset:512
	v_bitop3_b32 v7, v54, v55, 2 bitop3:0x36
	v_lshlrev_b32_e32 v7, 4, v7
	v_and_or_b32 v176, v7, 48, v6
	v_add_u32_e32 v174, 0, v176
	ds_read_b128 v[18:21], v174
	ds_read_b128 v[38:41], v174 offset:512
	s_mov_b32 s33, 0x41200000
	s_cmp_lg_u32 0, -1
	s_cselect_b32 s37, 0, 0
	s_waitcnt vmcnt(2) lgkmcnt(0)
	v_mfma_f32_32x32x16_f16 v[2:17], v[2:5], v[156:159], 0
	s_movk_i32 s4, 0x110
	v_and_b32_e32 v161, 63, v0
	v_lshl_or_b32 v1, v55, 8, v1
	s_mov_b32 s18, s5
	s_mov_b32 s19, s5
	s_mov_b32 s6, s5
	s_mov_b32 s7, s5
	v_mfma_f32_32x32x16_f16 v[2:17], v[18:21], v[152:155], v[2:17]
	ds_read_b128 v[18:21], v172 offset:8192
	ds_read_b128 v[42:45], v172 offset:8704
	ds_read_b128 v[46:49], v174 offset:8192
	ds_read_b128 v[50:53], v174 offset:8704
	s_mov_b32 s8, s5
	s_mov_b32 s9, s5
	s_mov_b32 s10, s5
	s_mov_b32 s11, s5
	s_mov_b32 s12, s5
	s_waitcnt lgkmcnt(3)
	v_mfma_f32_32x32x16_f16 v[18:33], v[18:21], v[156:159], 0
	s_mov_b32 s13, s5
	s_mov_b32 s14, s5
	s_mov_b32 s15, s5
	s_mov_b32 s16, s5
	s_mov_b32 s17, s5
	s_mov_b32 s36, 1
	s_mov_b32 s34, -1
	s_waitcnt lgkmcnt(1)
	v_mfma_f32_32x32x16_f16 v[18:33], v[46:49], v[152:155], v[18:33]
	s_mov_b32 s35, 2
	s_mov_b64 s[30:31], 0x8000
	v_mfma_f32_32x32x16_f16 v[2:17], v[34:37], v[148:151], v[2:17]
	v_mfma_f32_32x32x16_f16 v[18:33], v[42:45], v[148:151], v[18:33]
	v_mfma_f32_32x32x16_f16 v[2:17], v[38:41], v[144:147], v[2:17]
	ds_read_b128 v[34:37], v172 offset:1024
	ds_read_b128 v[38:41], v172 offset:1536
	s_waitcnt lgkmcnt(2)
	v_mfma_f32_32x32x16_f16 v[18:33], v[50:53], v[144:147], v[18:33]
	s_waitcnt lgkmcnt(1)
	v_mfma_f32_32x32x16_f16 v[2:17], v[34:37], v[140:143], v[2:17]
	ds_read_b128 v[34:37], v172 offset:9216
	ds_read_b128 v[42:45], v172 offset:9728
	s_waitcnt lgkmcnt(1)
	v_mfma_f32_32x32x16_f16 v[18:33], v[34:37], v[140:143], v[18:33]
	ds_read_b128 v[34:37], v174 offset:1024
	ds_read_b128 v[46:49], v174 offset:1536
	s_waitcnt lgkmcnt(1)
	v_mfma_f32_32x32x16_f16 v[2:17], v[34:37], v[136:139], v[2:17]
	ds_read_b128 v[34:37], v174 offset:9216
	ds_read_b128 v[50:53], v174 offset:9728
	v_mfma_f32_32x32x16_f16 v[2:17], v[38:41], v[132:135], v[2:17]
	s_waitcnt lgkmcnt(1)
	v_mfma_f32_32x32x16_f16 v[18:33], v[34:37], v[136:139], v[18:33]
	v_mov_b32_e32 v34, 0xf149f2ca
	v_mfma_f32_32x32x16_f16 v[2:17], v[46:49], v[128:131], v[2:17]
	v_mfma_f32_32x32x16_f16 v[18:33], v[42:45], v[132:135], v[18:33]
	s_nop 10
	v_max_f32_e32 v35, v3, v3
	v_max_f32_e32 v36, v2, v2
	v_max_f32_e32 v35, v36, v35
	v_max3_f32 v35, v35, v4, v5
	v_max3_f32 v35, v35, v6, v7
	v_max3_f32 v35, v35, v8, v9
	v_max3_f32 v35, v35, v10, v11
	s_waitcnt lgkmcnt(0)
	v_mfma_f32_32x32x16_f16 v[18:33], v[50:53], v[128:131], v[18:33]
	v_max3_f32 v35, v35, v12, v13
	v_max3_f32 v35, v35, v14, v15
	v_max3_f32 v35, v35, v16, v17
	s_nop 8
	v_max3_f32 v35, v35, v18, v19
	v_max3_f32 v35, v35, v20, v21
	v_max3_f32 v35, v35, v22, v23
	v_max3_f32 v35, v35, v24, v25
	v_max3_f32 v35, v35, v26, v27
	v_max3_f32 v35, v35, v28, v29
	v_max3_f32 v35, v35, v30, v31
	v_max3_f32 v35, v35, v32, v33
	v_mov_b32_e32 v36, v35
	s_nop 1
	v_permlane32_swap_b32_e32 v35, v36
	v_max_f32_e32 v36, v36, v36
	v_max_f32_e32 v35, v35, v35
	v_max_f32_e32 v35, v35, v36
	v_add_f32_e32 v36, 0x7149f2ca, v35
	v_cmp_ge_f32_e32 vcc, s33, v36
	s_cmp_eq_u64 vcc, exec
	v_max_f32_e32 v35, 0xf149f2ca, v35
	s_cselect_b64 vcc, -1, 0
	v_cndmask_b32_e32 v168, v35, v34, vcc
	v_sub_f32_e32 v96, v18, v168
	v_sub_f32_e32 v97, v19, v168
	v_lshlrev_b32_e32 v18, 4, v0
	v_lshrrev_b32_e32 v19, 4, v0
	v_sub_f32_e32 v98, v20, v168
	v_and_b32_e32 v18, 0xc0, v18
	v_bitop3_b32 v19, v19, v54, 1 bitop3:0x6c
	v_lshlrev_b32_e32 v20, 3, v0
	v_sub_f32_e32 v99, v21, v168
	v_lshl_or_b32 v18, v54, 11, v18
	v_lshlrev_b32_e32 v19, 5, v19
	v_and_b32_e32 v21, 8, v20
	v_or3_b32 v18, v18, v21, v19
	v_and_b32_e32 v19, 16, v20
	v_sub_f32_e32 v0, 0xf149f2ca, v35
	v_add3_u32 v163, v19, s37, v18
	v_bitop3_b32 v169, v18, s4, v19 bitop3:0x36
	v_exp_f32_e32 v18, v0
	s_add_u32 s2, s2, s20
	v_sub_f32_e32 v2, v2, v168
	v_sub_f32_e32 v3, v3, v168
	v_sub_f32_e32 v4, v4, v168
	v_sub_f32_e32 v5, v5, v168
	v_sub_f32_e32 v6, v6, v168
	v_sub_f32_e32 v7, v7, v168
	v_sub_f32_e32 v8, v8, v168
	v_sub_f32_e32 v9, v9, v168
	v_sub_f32_e32 v10, v10, v168
	v_sub_f32_e32 v11, v11, v168
	v_sub_f32_e32 v12, v12, v168
	v_sub_f32_e32 v13, v13, v168
	v_sub_f32_e32 v14, v14, v168
	v_sub_f32_e32 v15, v15, v168
	v_sub_f32_e32 v16, v16, v168
	v_sub_f32_e32 v17, v17, v168
	s_addc_u32 s3, s3, s21
	s_mov_b32 s4, s5
	v_exp_f32_e32 v127, v2
	v_exp_f32_e32 v180, v3
	v_exp_f32_e32 v125, v4
	v_exp_f32_e32 v179, v5
	v_exp_f32_e32 v123, v6
	v_exp_f32_e32 v126, v7
	v_exp_f32_e32 v122, v8
	v_exp_f32_e32 v124, v9
	v_exp_f32_e32 v119, v10
	v_exp_f32_e32 v121, v11
	v_exp_f32_e32 v117, v12
	v_exp_f32_e32 v120, v13
	v_exp_f32_e32 v115, v14
	v_exp_f32_e32 v118, v15
	v_exp_f32_e32 v114, v16
	v_exp_f32_e32 v116, v17
	v_or3_b32 v0, s2, v1, v164
	v_mov_b32_e32 v1, s3
	v_lshlrev_b32_e32 v164, 3, v54
	v_mov_b64_e32 v[62:63], s[18:19]
	v_lshl_add_u64 v[0:1], s[22:23], 0, v[0:1]
	s_mov_b64 s[2:3], 0xc080
	v_mov_b64_e32 v[48:49], s[4:5]
	v_sub_f32_e32 v100, v22, v168
	v_sub_f32_e32 v101, v23, v168
	v_sub_f32_e32 v102, v24, v168
	v_sub_f32_e32 v103, v25, v168
	v_sub_f32_e32 v104, v26, v168
	v_sub_f32_e32 v105, v27, v168
	v_sub_f32_e32 v106, v28, v168
	v_sub_f32_e32 v107, v29, v168
	v_sub_f32_e32 v108, v30, v168
	v_sub_f32_e32 v109, v31, v168
	v_sub_f32_e32 v110, v32, v168
	v_sub_f32_e32 v111, v33, v168
	v_lshl_add_u64 v[170:171], v[0:1], 0, s[2:3]
	s_movk_i32 s2, 0xbf80
	s_movk_i32 s20, 0xc000
	s_movk_i32 s22, 0xff80
	v_mov_b32_e32 v166, 1.0
	v_mov_b64_e32 v[60:61], s[16:17]
	v_mov_b64_e32 v[58:59], s[14:15]
	v_mov_b64_e32 v[56:57], s[12:13]
	v_mov_b64_e32 v[54:55], s[10:11]
	v_mov_b64_e32 v[52:53], s[8:9]
	v_mov_b64_e32 v[50:51], s[6:7]
	v_mov_b64_e32 v[32:33], v[48:49]
	v_mov_b64_e32 v[16:17], v[48:49]
	v_mov_b64_e32 v[0:1], v[48:49]
	s_mov_b32 s3, -1
	s_mov_b32 s21, -1
	s_mov_b32 s23, -1
	v_add_u32_e32 v167, s37, v169
	v_mov_b64_e32 v[34:35], v[50:51]
	v_mov_b64_e32 v[36:37], v[52:53]
	v_mov_b64_e32 v[38:39], v[54:55]
	v_mov_b64_e32 v[40:41], v[56:57]
	v_mov_b64_e32 v[42:43], v[58:59]
	v_mov_b64_e32 v[44:45], v[60:61]
	v_mov_b64_e32 v[46:47], v[62:63]
	v_mov_b64_e32 v[18:19], v[50:51]
	v_mov_b64_e32 v[20:21], v[52:53]
	v_mov_b64_e32 v[22:23], v[54:55]
	v_mov_b64_e32 v[24:25], v[56:57]
	v_mov_b64_e32 v[26:27], v[58:59]
	v_mov_b64_e32 v[28:29], v[60:61]
	v_mov_b64_e32 v[30:31], v[62:63]
	v_mov_b64_e32 v[2:3], v[50:51]
	v_mov_b64_e32 v[4:5], v[52:53]
	v_mov_b64_e32 v[6:7], v[54:55]
	v_mov_b64_e32 v[8:9], v[56:57]
	v_mov_b64_e32 v[10:11], v[58:59]
	v_mov_b64_e32 v[12:13], v[60:61]
	v_mov_b64_e32 v[14:15], v[62:63]
	s_nop 0
	s_nop 0
	s_nop 0
	s_nop 0
	s_nop 0
	s_nop 0
	s_nop 0
	s_nop 0
	s_nop 0
	s_nop 0
	s_nop 0
	s_nop 0
